# speedup vs baseline: 1.0337x; 1.0135x over previous
_Z11main_kernelPKDv8_DF16bS1_PKfS3_S3_PKiPKtS3_S3_Pf:
	s_lshl_b32 s14, s2, 5
	s_load_dwordx4 s[4:7], s[0:1], 0x0
	s_load_dwordx2 s[36:37], s[0:1], 0x10
	s_load_dwordx4 s[8:11], s[0:1], 0x28
	s_and_b32 s3, s14, 0xe0
	s_lshr_b32 s33, s2, 3
	s_or_b32 s15, s3, s33
	v_lshrrev_b32_e32 v73, 6, v0
	s_lshl_b32 s34, s15, 3
	v_or_b32_e32 v54, s34, v73
	v_mov_b32_e32 v55, 0
	v_and_b32_e32 v1, 63, v0
	v_lshlrev_b64 v[2:3], 7, v[54:55]
	s_waitcnt lgkmcnt(0)
	v_lshl_add_u64 v[2:3], s[10:11], 0, v[2:3]
	v_lshlrev_b32_e32 v4, 1, v1
	v_mov_b32_e32 v5, v55
	v_lshl_add_u64 v[2:3], v[2:3], 0, v[4:5]
	global_load_ushort v72, v[2:3], off
	v_and_b32_e32 v2, 7, v0
	v_bfe_u32 v74, v0, 4, 2
	v_lshlrev_b32_e32 v2, 4, v2
	s_mov_b32 s13, 0
	s_lshl_b32 s2, s15, 1
	s_lshl_b32 s12, s15, 2
	v_lshl_or_b32 v2, v74, 7, v2
	v_mov_b32_e32 v3, v55
	s_and_b32 s10, s2, 0x3ffffffc
	v_lshl_add_u64 v[58:59], s[4:5], 0, v[2:3]
	s_lshl_b64 s[2:3], s[12:13], 9
	v_lshl_add_u64 v[2:3], v[58:59], 0, s[2:3]
	s_or_b32 s2, s12, 1
	s_mov_b32 s3, s13
	s_lshl_b64 s[2:3], s[2:3], 9
	v_lshl_add_u64 v[4:5], v[58:59], 0, s[2:3]
	s_or_b32 s2, s12, 2
	s_mov_b32 s3, s13
	s_lshl_b64 s[2:3], s[2:3], 9
	s_mov_b32 exec_lo, 0xff00ff
	s_mov_b32 exec_hi, 0xff00ff
	global_load_dwordx4 v[22:25], v[2:3], off
	global_load_dwordx4 v[50:53], v[4:5], off
	s_mov_b64 exec, -1
	v_lshl_add_u64 v[2:3], v[58:59], 0, s[2:3]
	s_or_b32 s2, s12, 3
	s_mov_b32 s3, s13
	s_lshl_b64 s[2:3], s[2:3], 9
	v_lshl_add_u64 v[4:5], v[58:59], 0, s[2:3]
	s_and_b32 s2, s14, 0x700
	s_add_i32 s5, s33, 1
	s_lshl_b32 s14, s2, 4
	s_lshl_b32 s2, s5, 8
	s_and_b32 s2, s2, 0x700
	s_add_i32 s38, s33, 2
	s_lshl_b32 s16, s2, 4
	s_lshl_b32 s2, s38, 8
	s_and_b32 s2, s2, 0x700
	s_add_i32 s39, s33, 3
	s_lshl_b32 s18, s2, 4
	s_lshl_b32 s2, s39, 8
	s_and_b32 s44, s15, 0x1fffff80
	v_lshlrev_b32_e32 v75, 3, v73
	s_and_b32 s2, s2, 0x700
	s_add_i32 s40, s33, 4
	s_mov_b32 exec_lo, 0xff00ff
	s_mov_b32 exec_hi, 0xff00ff
	global_load_dwordx4 v[60:63], v[2:3], off
	global_load_dwordx4 v[64:67], v[4:5], off
	s_mov_b64 exec, -1
	v_or_b32_e32 v2, s44, v75
	v_mov_b32_e32 v3, v55
	s_lshl_b32 s20, s2, 4
	s_lshl_b32 s2, s40, 8
	v_lshlrev_b64 v[2:3], 12, v[2:3]
	s_and_b32 s2, s2, 0x700
	s_add_i32 s41, s33, 5
	v_lshl_add_u64 v[2:3], s[6:7], 0, v[2:3]
	v_lshlrev_b32_e32 v56, 4, v1
	v_mov_b32_e32 v57, v55
	s_lshl_b32 s22, s2, 4
	s_lshl_b32 s2, s41, 8
	v_lshl_add_u64 v[2:3], v[2:3], 0, v[56:57]
	s_mov_b32 s15, s13
	s_and_b32 s2, s2, 0x700
	s_add_i32 s42, s33, 6
	v_lshl_add_u64 v[4:5], v[2:3], 0, s[14:15]
	s_mov_b32 s17, s13
	s_lshl_b32 s24, s2, 4
	s_lshl_b32 s2, s42, 8
	global_load_dwordx4 v[18:21], v[4:5], off
	global_load_dwordx4 v[26:29], v[4:5], off offset:1024
	global_load_dwordx4 v[30:33], v[4:5], off offset:2048
	global_load_dwordx4 v[34:37], v[4:5], off offset:3072
	v_lshl_add_u64 v[4:5], v[2:3], 0, s[16:17]
	s_mov_b32 s19, s13
	s_and_b32 s2, s2, 0x700
	s_add_i32 s43, s33, 7
	global_load_dwordx4 v[38:41], v[4:5], off
	global_load_dwordx4 v[42:45], v[4:5], off offset:1024
	global_load_dwordx4 v[68:71], v[4:5], off offset:2048
	global_load_dwordx4 v[76:79], v[4:5], off offset:3072
	v_lshl_add_u64 v[4:5], v[2:3], 0, s[18:19]
	s_mov_b32 s21, s13
	s_lshl_b32 s26, s2, 4
	s_lshl_b32 s2, s43, 8
	global_load_dwordx4 v[80:83], v[4:5], off
	global_load_dwordx4 v[84:87], v[4:5], off offset:1024
	global_load_dwordx4 v[88:91], v[4:5], off offset:2048
	global_load_dwordx4 v[92:95], v[4:5], off offset:3072
	v_lshl_add_u64 v[4:5], v[2:3], 0, s[20:21]
	s_mov_b32 s23, s13
	s_and_b32 s2, s2, 0x700
	s_and_b32 s30, s34, 0x7ffffc00
	s_mov_b32 s31, s13
	global_load_dwordx4 v[96:99], v[4:5], off
	global_load_dwordx4 v[100:103], v[4:5], off offset:1024
	global_load_dwordx4 v[104:107], v[4:5], off offset:2048
	global_load_dwordx4 v[108:111], v[4:5], off offset:3072
	v_lshl_add_u64 v[4:5], v[2:3], 0, s[22:23]
	s_mov_b32 s25, s13
	s_lshl_b32 s28, s2, 4
	s_lshl_b64 s[2:3], s[30:31], 2
	global_load_dwordx4 v[112:115], v[4:5], off
	global_load_dwordx4 v[116:119], v[4:5], off offset:1024
	global_load_dwordx4 v[120:123], v[4:5], off offset:2048
	global_load_dwordx4 v[124:127], v[4:5], off offset:3072
	v_lshl_add_u64 v[4:5], v[2:3], 0, s[24:25]
	s_mov_b32 s27, s13
	s_mov_b32 s29, s13
	s_add_u32 s2, s36, s2
	global_load_dwordx4 v[128:131], v[4:5], off
	global_load_dwordx4 v[132:135], v[4:5], off offset:1024
	global_load_dwordx4 v[136:139], v[4:5], off offset:2048
	global_load_dwordx4 v[140:143], v[4:5], off offset:3072
	v_lshl_add_u64 v[4:5], v[2:3], 0, s[26:27]
	v_lshl_add_u64 v[2:3], v[2:3], 0, s[28:29]
	s_addc_u32 s3, s37, s3
	global_load_dwordx4 v[144:147], v[4:5], off
	global_load_dwordx4 v[148:151], v[4:5], off offset:1024
	global_load_dwordx4 v[152:155], v[4:5], off offset:2048
	global_load_dwordx4 v[156:159], v[4:5], off offset:3072
	global_load_dwordx4 v[160:163], v[2:3], off
	global_load_dwordx4 v[164:167], v[2:3], off offset:1024
	global_load_dwordx4 v[168:171], v[2:3], off offset:2048
	global_load_dwordx4 v[172:175], v[2:3], off offset:3072
	s_mov_b64 s[48:49], s[2:3]
	s_load_dwordx2 s[2:3], s[0:1], 0x40
	s_load_dword s15, s[8:9], s10 offset:0x0
	v_lshlrev_b32_e32 v1, 2, v1
	s_waitcnt lgkmcnt(0)
	s_load_dword s4, s[2:3], 0x0
	s_cmp_lg_u32 s15, 1
	s_cbranch_scc1 .Lmy_generic
	s_load_dwordx2 s[0:1], s[0:1], 0x48
	s_mov_b64 s[2:3], -1
	v_lshlrev_b32_e32 v176, 9, v73
	s_movk_i32 s6, 0x4040
	v_and_b32_e32 v177, 15, v0
	v_mad_u32_u24 v176, v74, s6, v176
	v_lshl_or_b32 v176, v177, 2, v176
	s_lshl_b32 s6, s33, 6
	s_and_b32 s6, s6, 0x1c0
	v_add_u32_e32 v177, s6, v176
	s_lshl_b32 s6, s5, 6
	s_and_b32 s6, s6, 0x1c0
	v_add_u32_e32 v178, s6, v176
	s_lshl_b32 s6, s38, 6
	s_and_b32 s6, s6, 0x1c0
	v_add_u32_e32 v179, s6, v176
	s_lshl_b32 s6, s39, 6
	s_and_b32 s6, s6, 0x1c0
	v_add_u32_e32 v180, s6, v176
	s_lshl_b32 s6, s40, 6
	s_and_b32 s6, s6, 0x1c0
	v_add_u32_e32 v181, s6, v176
	s_lshl_b32 s6, s41, 6
	s_and_b32 s6, s6, 0x1c0
	v_add_u32_e32 v182, s6, v176
	s_lshl_b32 s6, s42, 6
	s_and_b32 s6, s6, 0x1c0
	v_add_u32_e32 v183, s6, v176
	s_lshl_b32 s6, s43, 6
	s_and_b32 s6, s6, 0x1c0
	v_add_u32_e32 v184, s6, v176
	v_lshlrev_b32_e32 v186, 1, v1
	v_lshl_add_u32 v186, v73, 9, v186
	global_load_dwordx2 v[188:189], v186, s[48:49]
	s_waitcnt vmcnt(32)
	v_mfma_f32_16x16x32_bf16 v[18:21], v[22:25], v[18:21], 0
	s_waitcnt vmcnt(31)
	v_mfma_f32_16x16x32_bf16 v[18:21], v[50:53], v[26:29], v[18:21]
	s_waitcnt vmcnt(30)
	v_mfma_f32_16x16x32_bf16 v[18:21], v[60:63], v[30:33], v[18:21]
	s_waitcnt vmcnt(29)
	v_mfma_f32_16x16x32_bf16 v[46:49], v[64:67], v[34:37], v[18:21]
	s_waitcnt vmcnt(28)
	v_mfma_f32_16x16x32_bf16 v[18:21], v[22:25], v[38:41], 0
	s_waitcnt vmcnt(27)
	v_mfma_f32_16x16x32_bf16 v[18:21], v[50:53], v[42:45], v[18:21]
	s_waitcnt vmcnt(26)
	v_mfma_f32_16x16x32_bf16 v[18:21], v[60:63], v[68:71], v[18:21]
	s_waitcnt vmcnt(25)
	v_mfma_f32_16x16x32_bf16 v[42:45], v[64:67], v[76:79], v[18:21]
	ds_write_b32 v177, v46
	ds_write_b32 v177, v47 offset:4112
	ds_write_b32 v177, v48 offset:8224
	ds_write_b32 v177, v49 offset:12336
	s_waitcnt vmcnt(24)
	v_mfma_f32_16x16x32_bf16 v[18:21], v[22:25], v[80:83], 0
	s_waitcnt vmcnt(23)
	v_mfma_f32_16x16x32_bf16 v[18:21], v[50:53], v[84:87], v[18:21]
	s_waitcnt vmcnt(22)
	v_mfma_f32_16x16x32_bf16 v[18:21], v[60:63], v[88:91], v[18:21]
	s_waitcnt vmcnt(21)
	v_mfma_f32_16x16x32_bf16 v[38:41], v[64:67], v[92:95], v[18:21]
	ds_write_b32 v178, v42
	ds_write_b32 v178, v43 offset:4112
	ds_write_b32 v178, v44 offset:8224
	ds_write_b32 v178, v45 offset:12336
	s_waitcnt vmcnt(20)
	v_mfma_f32_16x16x32_bf16 v[18:21], v[22:25], v[96:99], 0
	s_waitcnt vmcnt(19)
	v_mfma_f32_16x16x32_bf16 v[18:21], v[50:53], v[100:103], v[18:21]
	s_waitcnt vmcnt(18)
	v_mfma_f32_16x16x32_bf16 v[18:21], v[60:63], v[104:107], v[18:21]
	s_waitcnt vmcnt(17)
	v_mfma_f32_16x16x32_bf16 v[34:37], v[64:67], v[108:111], v[18:21]
	ds_write_b32 v179, v38
	ds_write_b32 v179, v39 offset:4112
	ds_write_b32 v179, v40 offset:8224
	ds_write_b32 v179, v41 offset:12336
	s_waitcnt vmcnt(16)
	v_mfma_f32_16x16x32_bf16 v[18:21], v[22:25], v[112:115], 0
	s_waitcnt vmcnt(15)
	v_mfma_f32_16x16x32_bf16 v[18:21], v[50:53], v[116:119], v[18:21]
	s_waitcnt vmcnt(14)
	v_mfma_f32_16x16x32_bf16 v[18:21], v[60:63], v[120:123], v[18:21]
	s_waitcnt vmcnt(13)
	v_mfma_f32_16x16x32_bf16 v[30:33], v[64:67], v[124:127], v[18:21]
	ds_write_b32 v180, v34
	ds_write_b32 v180, v35 offset:4112
	ds_write_b32 v180, v36 offset:8224
	ds_write_b32 v180, v37 offset:12336
	s_waitcnt vmcnt(12)
	v_mfma_f32_16x16x32_bf16 v[18:21], v[22:25], v[128:131], 0
	s_waitcnt vmcnt(11)
	v_mfma_f32_16x16x32_bf16 v[18:21], v[50:53], v[132:135], v[18:21]
	s_waitcnt vmcnt(10)
	v_mfma_f32_16x16x32_bf16 v[18:21], v[60:63], v[136:139], v[18:21]
	s_waitcnt vmcnt(9)
	v_mfma_f32_16x16x32_bf16 v[26:29], v[64:67], v[140:143], v[18:21]
	ds_write_b32 v181, v30
	ds_write_b32 v181, v31 offset:4112
	ds_write_b32 v181, v32 offset:8224
	ds_write_b32 v181, v33 offset:12336
	s_waitcnt vmcnt(8)
	v_mfma_f32_16x16x32_bf16 v[18:21], v[22:25], v[144:147], 0
	s_waitcnt vmcnt(4)
	v_mfma_f32_16x16x32_bf16 v[22:25], v[22:25], v[160:163], 0
	v_mfma_f32_16x16x32_bf16 v[18:21], v[50:53], v[148:151], v[18:21]
	s_waitcnt vmcnt(3)
	v_mfma_f32_16x16x32_bf16 v[22:25], v[50:53], v[164:167], v[22:25]
	v_mfma_f32_16x16x32_bf16 v[18:21], v[60:63], v[152:155], v[18:21]
	s_waitcnt vmcnt(2)
	v_mfma_f32_16x16x32_bf16 v[22:25], v[60:63], v[168:171], v[22:25]
	ds_write_b32 v182, v26
	ds_write_b32 v182, v27 offset:4112
	ds_write_b32 v182, v28 offset:8224
	ds_write_b32 v182, v29 offset:12336
	v_mfma_f32_16x16x32_bf16 v[18:21], v[64:67], v[156:159], v[18:21]
	s_waitcnt vmcnt(1)
	v_mfma_f32_16x16x32_bf16 v[22:25], v[64:67], v[172:175], v[22:25]
	s_nop 7
	ds_write_b32 v183, v18
	ds_write_b32 v183, v19 offset:4112
	ds_write_b32 v183, v20 offset:8224
	ds_write_b32 v183, v21 offset:12336
	ds_write_b32 v184, v22
	ds_write_b32 v184, v23 offset:4112
	ds_write_b32 v184, v24 offset:8224
	ds_write_b32 v184, v25 offset:12336
	s_waitcnt vmcnt(0)
	v_add_u32_e32 v187, 0x10100, v186
	ds_write_b64 v187, v[188:189]
	s_movk_i32 s5, 0x1010
	v_mad_u32_u24 v0, v73, s5, v56
	v_add_u32_e32 v187, 0x10100, v56
	s_waitcnt lgkmcnt(0)
	s_barrier
	ds_read_b128 v[14:17], v187
	ds_read_b128 v[10:13], v187 offset:1024
	ds_read_b128 v[6:9], v187 offset:2048
	ds_read_b128 v[2:5], v187 offset:3072
	s_waitcnt lgkmcnt(0)
	s_branch .Lmy_tail
.Lmy_generic:
	global_load_dwordx4 v[14:17], v56, s[48:49]
	global_load_dwordx4 v[10:13], v56, s[48:49] offset:1024
	global_load_dwordx4 v[6:9], v56, s[48:49] offset:2048
	global_load_dwordx4 v[2:5], v56, s[48:49] offset:3072
	s_waitcnt vmcnt(35)
	v_mfma_f32_16x16x32_bf16 v[18:21], v[22:25], v[18:21], 0
	s_cmp_lt_i32 s15, 3
	s_cselect_b64 s[2:3], -1, 0
	s_mov_b64 s[8:9], -1
	s_waitcnt vmcnt(34)
	v_mfma_f32_16x16x32_bf16 v[18:21], v[50:53], v[26:29], v[18:21]
	s_and_b64 vcc, exec, s[2:3]
	s_waitcnt vmcnt(33)
	v_mfma_f32_16x16x32_bf16 v[18:21], v[60:63], v[30:33], v[18:21]
	s_waitcnt vmcnt(32)
	v_mfma_f32_16x16x32_bf16 v[46:49], v[64:67], v[34:37], v[18:21]
	s_waitcnt vmcnt(31)
	v_mfma_f32_16x16x32_bf16 v[18:21], v[22:25], v[38:41], 0
	s_waitcnt vmcnt(30)
	v_mfma_f32_16x16x32_bf16 v[18:21], v[50:53], v[42:45], v[18:21]
	s_waitcnt vmcnt(29)
	v_mfma_f32_16x16x32_bf16 v[18:21], v[60:63], v[68:71], v[18:21]
	s_waitcnt vmcnt(28)
	v_mfma_f32_16x16x32_bf16 v[42:45], v[64:67], v[76:79], v[18:21]
	s_waitcnt vmcnt(27)
	v_mfma_f32_16x16x32_bf16 v[18:21], v[22:25], v[80:83], 0
	s_waitcnt vmcnt(26)
	v_mfma_f32_16x16x32_bf16 v[18:21], v[50:53], v[84:87], v[18:21]
	s_waitcnt vmcnt(25)
	v_mfma_f32_16x16x32_bf16 v[18:21], v[60:63], v[88:91], v[18:21]
	s_waitcnt vmcnt(24)
	v_mfma_f32_16x16x32_bf16 v[38:41], v[64:67], v[92:95], v[18:21]
	s_waitcnt vmcnt(23)
	v_mfma_f32_16x16x32_bf16 v[18:21], v[22:25], v[96:99], 0
	s_waitcnt vmcnt(22)
	v_mfma_f32_16x16x32_bf16 v[18:21], v[50:53], v[100:103], v[18:21]
	s_waitcnt vmcnt(21)
	v_mfma_f32_16x16x32_bf16 v[18:21], v[60:63], v[104:107], v[18:21]
	s_waitcnt vmcnt(20)
	v_mfma_f32_16x16x32_bf16 v[34:37], v[64:67], v[108:111], v[18:21]
	s_waitcnt vmcnt(19)
	v_mfma_f32_16x16x32_bf16 v[18:21], v[22:25], v[112:115], 0
	s_waitcnt vmcnt(18)
	v_mfma_f32_16x16x32_bf16 v[18:21], v[50:53], v[116:119], v[18:21]
	s_waitcnt vmcnt(17)
	v_mfma_f32_16x16x32_bf16 v[18:21], v[60:63], v[120:123], v[18:21]
	s_waitcnt vmcnt(16)
	v_mfma_f32_16x16x32_bf16 v[30:33], v[64:67], v[124:127], v[18:21]
	s_waitcnt vmcnt(15)
	v_mfma_f32_16x16x32_bf16 v[18:21], v[22:25], v[128:131], 0
	s_waitcnt vmcnt(14)
	v_mfma_f32_16x16x32_bf16 v[18:21], v[50:53], v[132:135], v[18:21]
	s_waitcnt vmcnt(13)
	v_mfma_f32_16x16x32_bf16 v[18:21], v[60:63], v[136:139], v[18:21]
	s_waitcnt vmcnt(12)
	v_mfma_f32_16x16x32_bf16 v[26:29], v[64:67], v[140:143], v[18:21]
	s_waitcnt vmcnt(11)
	v_mfma_f32_16x16x32_bf16 v[18:21], v[22:25], v[144:147], 0
	s_waitcnt vmcnt(7)
	v_mfma_f32_16x16x32_bf16 v[22:25], v[22:25], v[160:163], 0
	v_mfma_f32_16x16x32_bf16 v[18:21], v[50:53], v[148:151], v[18:21]
	s_waitcnt vmcnt(6)
	v_mfma_f32_16x16x32_bf16 v[22:25], v[50:53], v[164:167], v[22:25]
	v_mfma_f32_16x16x32_bf16 v[18:21], v[60:63], v[152:155], v[18:21]
	s_waitcnt vmcnt(5)
	v_mfma_f32_16x16x32_bf16 v[22:25], v[60:63], v[168:171], v[22:25]
	v_mfma_f32_16x16x32_bf16 v[18:21], v[64:67], v[156:159], v[18:21]
	s_waitcnt vmcnt(4)
	v_mfma_f32_16x16x32_bf16 v[22:25], v[64:67], v[172:175], v[22:25]
	s_cbranch_vccz .LBB1_5
	s_load_dwordx2 s[0:1], s[0:1], 0x48
	s_and_b64 vcc, exec, s[8:9]
	s_cbranch_vccz .LBB1_4
	s_cmp_lg_u32 s15, 2
	s_cbranch_scc0 .LBB1_14

.Lmy_tail:
	ds_read_b128 v[18:21], v0
	s_waitcnt vmcnt(3)
	v_pk_add_f32 v[22:23], s[4:5], v[16:17] op_sel_hi:[0,1]
	v_pk_add_f32 v[24:25], s[4:5], v[14:15] op_sel_hi:[0,1]
	ds_read_b128 v[14:17], v0 offset:1024
	s_waitcnt vmcnt(2)
	v_pk_add_f32 v[12:13], s[4:5], v[12:13] op_sel_hi:[0,1]
	s_waitcnt lgkmcnt(1)
	v_pk_add_f32 v[22:23], v[20:21], v[22:23]
	v_pk_add_f32 v[24:25], v[18:19], v[24:25]
	v_pk_add_f32 v[10:11], s[4:5], v[10:11] op_sel_hi:[0,1]
	v_cndmask_b32_e64 v21, v21, v23, s[2:3]
	v_cndmask_b32_e64 v20, v20, v22, s[2:3]
	v_cndmask_b32_e64 v22, v19, v25, s[2:3]
	v_cndmask_b32_e64 v23, v18, v24, s[2:3]
	s_waitcnt lgkmcnt(0)
	v_pk_add_f32 v[12:13], v[16:17], v[12:13]
	v_pk_add_f32 v[18:19], v[14:15], v[10:11]
	v_cndmask_b32_e64 v24, v17, v13, s[2:3]
	v_cndmask_b32_e64 v25, v16, v12, s[2:3]
	v_cndmask_b32_e64 v19, v15, v19, s[2:3]
	ds_read_b128 v[10:13], v0 offset:2048
	v_cndmask_b32_e64 v18, v14, v18, s[2:3]
	s_waitcnt vmcnt(1)
	v_pk_add_f32 v[14:15], s[4:5], v[8:9] op_sel_hi:[0,1]
	v_pk_add_f32 v[16:17], s[4:5], v[6:7] op_sel_hi:[0,1]
	ds_read_b128 v[6:9], v0 offset:3072
	s_waitcnt vmcnt(0)
	v_pk_add_f32 v[4:5], s[4:5], v[4:5] op_sel_hi:[0,1]
	v_cmp_ne_u16_e32 vcc, 0, v72
	s_cmp_lg_u64 vcc, 0
	v_and_b32_e32 v26, 0xffff, v72
	s_waitcnt lgkmcnt(0)
	v_pk_add_f32 v[4:5], v[8:9], v[4:5]
	s_cselect_b64 vcc, -1, 0
	v_cndmask_b32_e64 v4, v8, v4, s[2:3]
	v_mov_b32_e32 v8, 0xffff
	v_pk_add_f32 v[14:15], v[12:13], v[14:15]
	v_cndmask_b32_e32 v8, v8, v26, vcc
	v_cndmask_b32_e64 v0, v13, v15, s[2:3]
	v_and_b32_e32 v13, 1, v8
	v_pk_add_f32 v[16:17], v[10:11], v[16:17]
	v_cndmask_b32_e64 v12, v12, v14, s[2:3]
	v_cndmask_b32_e64 v5, v9, v5, s[2:3]
	v_mul_f32_e32 v9, 0x3fb8aa3b, v23
	v_mov_b32_e32 v14, 0xff800000
	v_cmp_eq_u32_e32 vcc, 1, v13
	v_and_b32_e32 v15, 2, v8
	v_cndmask_b32_e64 v11, v11, v17, s[2:3]
	v_cndmask_b32_e32 v9, v14, v9, vcc
	v_mul_f32_e32 v13, 0x3fb8aa3b, v22
	v_cmp_ne_u32_e32 vcc, 0, v15
	v_and_b32_e32 v17, 4, v8
	v_cndmask_b32_e64 v10, v10, v16, s[2:3]
	v_cndmask_b32_e32 v13, v14, v13, vcc
	v_mul_f32_e32 v16, 0x3fb8aa3b, v20
	v_cmp_ne_u32_e32 vcc, 0, v17
	v_and_b32_e32 v20, 8, v8
	v_mul_f32_e32 v17, 0x3fb8aa3b, v21
	v_cndmask_b32_e32 v16, v14, v16, vcc
	v_cmp_ne_u32_e32 vcc, 0, v20
	v_and_b32_e32 v20, 16, v8
	v_pk_add_f32 v[2:3], s[4:5], v[2:3] op_sel_hi:[0,1]
	v_cndmask_b32_e32 v17, v14, v17, vcc
	v_mul_f32_e32 v18, 0x3fb8aa3b, v18
	v_cmp_ne_u32_e32 vcc, 0, v20
	v_and_b32_e32 v20, 32, v8
	v_pk_add_f32 v[2:3], v[6:7], v[2:3]
	v_cndmask_b32_e32 v18, v14, v18, vcc
	v_mul_f32_e32 v19, 0x3fb8aa3b, v19
	v_cmp_ne_u32_e32 vcc, 0, v20
	v_and_b32_e32 v21, 64, v8
	v_cndmask_b32_e64 v7, v7, v3, s[2:3]
	v_cndmask_b32_e64 v6, v6, v2, s[2:3]
	v_lshlrev_b64 v[2:3], 12, v[54:55]
	v_cndmask_b32_e32 v19, v14, v19, vcc
	v_mul_f32_e32 v20, 0x3fb8aa3b, v25
	v_cmp_ne_u32_e32 vcc, 0, v21
	v_and_b32_e32 v22, 0x80, v8
	v_lshl_add_u64 v[2:3], s[0:1], 0, v[2:3]
	s_mov_b32 s0, 0xff800000
	v_cndmask_b32_e32 v20, v14, v20, vcc
	v_mul_f32_e32 v21, 0x3fb8aa3b, v24
	v_cmp_ne_u32_e32 vcc, 0, v22
	v_and_b32_e32 v22, 0x100, v8
	v_max3_f32 v15, v9, s0, v13
	v_cndmask_b32_e32 v21, v14, v21, vcc
	v_mul_f32_e32 v10, 0x3fb8aa3b, v10
	v_cmp_ne_u32_e32 vcc, 0, v22
	v_max3_f32 v15, v15, v16, v17
	v_max3_f32 v15, v15, v18, v19
	v_cndmask_b32_e32 v22, v14, v10, vcc
	v_mul_f32_e32 v10, 0x3fb8aa3b, v11
	v_and_b32_e32 v11, 0x200, v8
	v_cmp_ne_u32_e32 vcc, 0, v11
	v_mul_f32_e32 v11, 0x3fb8aa3b, v12
	v_and_b32_e32 v12, 0x400, v8
	v_max3_f32 v15, v15, v20, v21
	v_cndmask_b32_e32 v23, v14, v10, vcc
	v_cmp_ne_u32_e32 vcc, 0, v12
	v_max3_f32 v10, v15, v22, v23
	v_mul_f32_e32 v0, 0x3fb8aa3b, v0
	v_cndmask_b32_e32 v15, v14, v11, vcc
	v_and_b32_e32 v11, 0x800, v8
	v_cmp_ne_u32_e32 vcc, 0, v11
	v_and_b32_e32 v11, 0x1000, v8
	v_mul_f32_e32 v6, 0x3fb8aa3b, v6
	v_cndmask_b32_e32 v0, v14, v0, vcc
	v_cmp_ne_u32_e32 vcc, 0, v11
	v_mul_f32_e32 v4, 0x3fb8aa3b, v4
	s_movk_i32 s0, 0x7fff
	v_cndmask_b32_e32 v24, v14, v6, vcc
	v_mul_f32_e32 v6, 0x3fb8aa3b, v7
	v_and_b32_e32 v7, 0x2000, v8
	v_cmp_ne_u32_e32 vcc, 0, v7
	v_and_b32_e32 v7, 0x4000, v8
	v_max3_f32 v10, v10, v15, v0
	v_cndmask_b32_e32 v25, v14, v6, vcc
	v_cmp_ne_u32_e32 vcc, 0, v7
	v_max3_f32 v6, v10, v24, v25
	s_nop 0
	v_cndmask_b32_e32 v26, v14, v4, vcc
	v_mul_f32_e32 v4, 0x3fb8aa3b, v5
	v_cmp_lt_u32_e32 vcc, s0, v8
	v_mov_b32_e32 v5, 0
	s_nop 0
	v_cndmask_b32_e32 v27, v14, v4, vcc
	v_max3_f32 v4, v6, v26, v27
	s_nop 1
	v_mov_b32_dpp v5, v4 quad_perm:[1,0,3,2] row_mask:0xf bank_mask:0xf
	v_max_f32_e32 v5, v5, v5
	v_max_f32_e32 v4, v4, v5
	v_mov_b32_e32 v5, 0
	s_nop 1
	v_mov_b32_dpp v5, v4 quad_perm:[2,3,0,1] row_mask:0xf bank_mask:0xf
	v_max_f32_e32 v5, v5, v5
	v_max_f32_e32 v4, v4, v5
	v_mov_b32_e32 v5, 0
	s_nop 1
	v_mov_b32_dpp v5, v4 row_half_mirror row_mask:0xf bank_mask:0xf
	v_max_f32_e32 v5, v5, v5
	v_max_f32_e32 v4, v4, v5
	v_mov_b32_e32 v5, 0
	s_nop 1
	v_mov_b32_dpp v5, v4 row_mirror row_mask:0xf bank_mask:0xf
	v_max_f32_e32 v5, v5, v5
	v_max_f32_e32 v4, v4, v5
	s_nop 0
	v_readlane_b32 s2, v4, 32
	v_readlane_b32 s3, v4, 48
	v_readlane_b32 s0, v4, 0
	v_readlane_b32 s1, v4, 16
	v_max_f32_e64 v4, s3, s3
	v_max_f32_e64 v5, s2, s2
	v_max_f32_e32 v4, v5, v4
	v_mov_b32_e32 v5, s1
	v_max3_f32 v28, s0, v5, v4
	v_sub_f32_e32 v4, v9, v28
	v_exp_f32_e32 v4, v4
	v_sub_f32_e32 v5, v13, v28
	v_exp_f32_e32 v5, v5
	v_sub_f32_e32 v6, v16, v28
	v_exp_f32_e32 v6, v6
	v_sub_f32_e32 v7, v17, v28
	v_exp_f32_e32 v7, v7
	v_add_f32_e32 v8, 0, v4
	v_add_f32_e32 v8, v8, v5
	v_add_f32_e32 v8, v8, v6
	v_add_f32_e32 v12, v8, v7
	v_sub_f32_e32 v8, v18, v28
	v_exp_f32_e32 v8, v8
	v_sub_f32_e32 v9, v19, v28
	v_exp_f32_e32 v9, v9
	v_sub_f32_e32 v10, v20, v28
	v_exp_f32_e32 v10, v10
	v_sub_f32_e32 v11, v21, v28
	v_exp_f32_e32 v11, v11
	v_add_f32_e32 v12, v12, v8
	v_add_f32_e32 v12, v12, v9
	v_add_f32_e32 v12, v12, v10
	v_add_f32_e32 v16, v12, v11
	v_sub_f32_e32 v12, v22, v28
	v_exp_f32_e32 v12, v12
	v_sub_f32_e32 v13, v23, v28
	v_exp_f32_e32 v13, v13
	v_sub_f32_e32 v14, v15, v28
	v_exp_f32_e32 v14, v14
	v_sub_f32_e32 v0, v0, v28
	v_exp_f32_e32 v15, v0
	v_add_f32_e32 v0, v16, v12
	v_sub_f32_e32 v16, v24, v28
	v_exp_f32_e32 v16, v16
	v_sub_f32_e32 v17, v25, v28
	v_add_f32_e32 v0, v0, v13
	v_exp_f32_e32 v17, v17
	v_sub_f32_e32 v18, v26, v28
	v_add_f32_e32 v0, v0, v14
	v_exp_f32_e32 v18, v18
	v_sub_f32_e32 v19, v27, v28
	v_add_f32_e32 v0, v0, v15
	v_exp_f32_e32 v19, v19
	v_add_f32_e32 v0, v0, v16
	v_add_f32_e32 v0, v0, v17
	v_add_f32_e32 v0, v0, v18
	v_add_f32_e32 v0, v0, v19
	s_nop 1
	v_add_f32_dpp v0, v0, v0 quad_perm:[1,0,3,2] row_mask:0xf bank_mask:0xf bound_ctrl:1
	s_nop 1
	v_add_f32_dpp v0, v0, v0 quad_perm:[2,3,0,1] row_mask:0xf bank_mask:0xf bound_ctrl:1
	s_nop 1
	v_add_f32_dpp v0, v0, v0 row_half_mirror row_mask:0xf bank_mask:0xf bound_ctrl:1
	s_nop 1
	v_add_f32_dpp v0, v0, v0 row_mirror row_mask:0xf bank_mask:0xf bound_ctrl:1
	s_nop 0
	v_readlane_b32 s2, v0, 16
	v_readlane_b32 s3, v0, 48
	v_readlane_b32 s0, v0, 0
	v_readlane_b32 s1, v0, 32
	v_mov_b32_e32 v20, s2
	v_mov_b32_e32 v21, s3
	v_pk_add_f32 v[20:21], s[0:1], v[20:21]
	s_nop 0
	v_add_f32_e32 v0, v20, v21
	v_div_scale_f32 v22, s[0:1], v0, v0, 1.0
	v_rcp_f32_e32 v23, v22
	v_lshlrev_b32_e32 v20, 2, v1
	v_mov_b32_e32 v21, 0
	v_lshl_add_u64 v[20:21], v[2:3], 0, v[20:21]
	v_fma_f32 v1, -v22, v23, 1.0
	v_fmac_f32_e32 v23, v1, v23
	v_div_scale_f32 v1, vcc, 1.0, v0, 1.0
	v_mul_f32_e32 v2, v1, v23
	v_fma_f32 v3, -v22, v2, v1
	v_fmac_f32_e32 v2, v3, v23
	v_fma_f32 v1, -v22, v2, v1
	v_div_fmas_f32 v1, v1, v23, v2
	v_div_fixup_f32 v22, v1, v0, 1.0
	v_pk_mul_f32 v[2:3], v[22:23], v[6:7] op_sel_hi:[0,1]
	v_pk_mul_f32 v[0:1], v[22:23], v[4:5] op_sel_hi:[0,1]
	global_store_dwordx4 v[20:21], v[0:3], off sc1
	s_nop 1
	v_pk_mul_f32 v[2:3], v[22:23], v[10:11] op_sel_hi:[0,1]
	v_pk_mul_f32 v[0:1], v[22:23], v[8:9] op_sel_hi:[0,1]
	global_store_dwordx4 v[20:21], v[0:3], off offset:1024 sc1
	s_nop 1
	v_pk_mul_f32 v[2:3], v[22:23], v[14:15] op_sel_hi:[0,1]
	v_pk_mul_f32 v[0:1], v[22:23], v[12:13] op_sel_hi:[0,1]
	global_store_dwordx4 v[20:21], v[0:3], off offset:2048 sc1
	s_nop 1
	v_pk_mul_f32 v[2:3], v[22:23], v[18:19] op_sel_hi:[0,1]
	v_pk_mul_f32 v[0:1], v[22:23], v[16:17] op_sel_hi:[0,1]
	global_store_dwordx4 v[20:21], v[0:3], off offset:3072 sc1
	s_endpgm
